# L1 dense attention epilogue: quad-transposed dword stores instead of 64 byte stores
# baseline (speedup 1.0000x reference)
; __device__ __forceinline__ bf16_t f2bf(float f) { return (bf16_t)(cvtpk(f, f) & 0xffffu); }
; __device__ __forceinline__ unsigned char f2fp8(float v) { return (unsigned char)(__builtin_amdgcn_cvt_pk_fp8_f32(v, v, (int)__float_as_uint(v), false) & 0xff); }
; __device__ __forceinline__ int fresh_tid(int wv) { int l; asm volatile("v_mbcnt_lo_u32_b32 %0, -1, 0\n\tv_mbcnt_hi_u32_b32 %0, -1, %0" : "=v"(l)); return wv * 64 + l; }
; __device__ __forceinline__ int crow(int r, int hi) { return (r & 3) + 8 * (r >> 2) + 4 * hi; }
; template <int NKS, bool MACC>
; __device__ __forceinline__ void attn_dense8_dma(int wv, const D8Args a, LAS unsigned char* ldsl) {
;     ...
;     const int tid_e = fresh_tid(wv), wid_e = tid_e >> 6, r32e = tid_e & 31, hie = (tid_e >> 5) & 1;
;     float* li_e = (float*)(lds + DM_WS) + wid_e * 64;
;     float rli[16];
;     if constexpr (LSUM) {
; #pragma unroll
;         for (int r = 0; r < 16; ++r) rli[r] = __builtin_amdgcn_rcpf(lacc[r]); (void)li_e; }
;     else { if (hie == 0) li_e[r32e] = l_reg; asm volatile("s_waitcnt lgkmcnt(0)" ::: "memory");
; #pragma unroll
;         for (int r = 0; r < 16; ++r) rli[r] = __builtin_amdgcn_rcpf(li_e[da::crow(r, hie)]); }
;     bf16_t* Ow = F8_OUT ? (bf16_t*)((unsigned char*)a.O + (long)(wid_e * 32) * a.ldo) : a.O + (long)(wid_e * 32) * a.ldo;
; #pragma unroll
;     for (int r = 0; r < 16; ++r) { const int orow = da::crow(r, hie);
; #pragma unroll
;         for (int d0 = 0; d0 < 4; ++d0) { if constexpr (F8_OUT) ((unsigned char*)Ow)[(long)orow * a.ldo + d0 * 32 + r32e] = f2fp8(o[d0][r] * rli[r] * O8_SCALE); else Ow[(long)orow * a.ldo + d0 * 32 + r32e] = f2bf(o[d0][r] * rli[r]); } }
.LBB0_454:
	s_or_b64 exec, exec, s[0:1]
	s_waitcnt lgkmcnt(0)
	v_lshl_add_u32 v64, v66, 4, v68
	ds_read_b128 v[68:71], v64
	ds_read_b128 v[72:75], v64 offset:32
	ds_read_b128 v[76:79], v64 offset:64
	ds_read_b128 v[80:83], v64 offset:96
	s_lshl_b64 s[0:1], s[34:35], 11
	s_add_u32 s0, s70, s0
	s_addc_u32 s1, s71, s1
	s_add_u32 s0, s0, s55
	s_addc_u32 s1, s1, 0
	v_lshrrev_b32_e32 v64, 6, v67
	v_lshlrev_b32_e32 v64, 5, v64
	v_lshl_add_u32 v64, v66, 2, v64
	v_and_b32_e32 v65, 3, v232
	v_add_u32_e32 v64, v64, v65
	v_lshlrev_b32_e32 v64, 11, v64
	v_lshrrev_b32_e32 v65, 2, v232
	v_lshl_add_u32 v64, v65, 2, v64
	v_bfe_i32 v65, v232, 0, 1
	v_and_b32_e32 v65, 0x05050505, v65
	v_xor_b32_e32 v65, 0x06020400, v65
	v_bfe_i32 v66, v232, 1, 1
	v_and_b32_e32 v66, 0x06060606, v66
	v_xor_b32_e32 v66, 0x05040100, v66
	s_waitcnt lgkmcnt(0)
	v_rcp_f32_e32 v68, v68
	v_rcp_f32_e32 v69, v69
	v_rcp_f32_e32 v70, v70
	v_rcp_f32_e32 v71, v71
	v_rcp_f32_e32 v72, v72
	v_rcp_f32_e32 v73, v73
	v_rcp_f32_e32 v74, v74
	v_rcp_f32_e32 v75, v75
	v_rcp_f32_e32 v76, v76
	v_rcp_f32_e32 v77, v77
	v_rcp_f32_e32 v78, v78
	v_rcp_f32_e32 v79, v79
	v_rcp_f32_e32 v80, v80
	v_rcp_f32_e32 v81, v81
	v_rcp_f32_e32 v82, v82
	v_rcp_f32_e32 v83, v83
	v_mul_f32_e32 v68, 0x41800000, v68
	v_mul_f32_e32 v69, 0x41800000, v69
	v_mul_f32_e32 v70, 0x41800000, v70
	v_mul_f32_e32 v71, 0x41800000, v71
	v_mul_f32_e32 v72, 0x41800000, v72
	v_mul_f32_e32 v73, 0x41800000, v73
	v_mul_f32_e32 v74, 0x41800000, v74
	v_mul_f32_e32 v75, 0x41800000, v75
	v_mul_f32_e32 v76, 0x41800000, v76
	v_mul_f32_e32 v77, 0x41800000, v77
	v_mul_f32_e32 v78, 0x41800000, v78
	v_mul_f32_e32 v79, 0x41800000, v79
	v_mul_f32_e32 v80, 0x41800000, v80
	v_mul_f32_e32 v81, 0x41800000, v81
	v_mul_f32_e32 v82, 0x41800000, v82
	v_mul_f32_e32 v83, 0x41800000, v83
	v_mul_f32_e32 v0, v0, v68
	v_mul_f32_e32 v16, v16, v68
	v_mul_f32_e32 v32, v32, v68
	v_mul_f32_e32 v48, v48, v68
	v_mul_f32_e32 v1, v1, v69
	v_mul_f32_e32 v17, v17, v69
	v_mul_f32_e32 v33, v33, v69
	v_mul_f32_e32 v49, v49, v69
	v_mul_f32_e32 v2, v2, v70
	v_mul_f32_e32 v18, v18, v70
	v_mul_f32_e32 v34, v34, v70
	v_mul_f32_e32 v50, v50, v70
	v_mul_f32_e32 v3, v3, v71
	v_mul_f32_e32 v19, v19, v71
	v_mul_f32_e32 v35, v35, v71
	v_mul_f32_e32 v51, v51, v71
	v_cvt_pk_fp8_f32 v0, v0, v1
	v_cvt_pk_fp8_f32 v16, v16, v17
	v_cvt_pk_fp8_f32 v32, v32, v33
	v_cvt_pk_fp8_f32 v48, v48, v49
	v_cvt_pk_fp8_f32 v0, v2, v3 op_sel:[0,0,1]
	v_cvt_pk_fp8_f32 v16, v18, v19 op_sel:[0,0,1]
	v_cvt_pk_fp8_f32 v32, v34, v35 op_sel:[0,0,1]
	v_cvt_pk_fp8_f32 v48, v50, v51 op_sel:[0,0,1]
	v_mov_b32_dpp v1, v0 quad_perm:[1,0,3,2] row_mask:0xf bank_mask:0xf
	v_mov_b32_dpp v17, v16 quad_perm:[1,0,3,2] row_mask:0xf bank_mask:0xf
	v_mov_b32_dpp v33, v32 quad_perm:[1,0,3,2] row_mask:0xf bank_mask:0xf
	v_mov_b32_dpp v49, v48 quad_perm:[1,0,3,2] row_mask:0xf bank_mask:0xf
	v_perm_b32 v2, v1, v0, v65
	v_perm_b32 v18, v17, v16, v65
	v_perm_b32 v34, v33, v32, v65
	v_perm_b32 v50, v49, v48, v65
	v_mov_b32_dpp v3, v2 quad_perm:[2,3,0,1] row_mask:0xf bank_mask:0xf
	v_mov_b32_dpp v19, v18 quad_perm:[2,3,0,1] row_mask:0xf bank_mask:0xf
	v_mov_b32_dpp v35, v34 quad_perm:[2,3,0,1] row_mask:0xf bank_mask:0xf
	v_mov_b32_dpp v51, v50 quad_perm:[2,3,0,1] row_mask:0xf bank_mask:0xf
	v_perm_b32 v0, v3, v2, v66
	v_perm_b32 v16, v19, v18, v66
	v_perm_b32 v32, v35, v34, v66
	v_perm_b32 v48, v51, v50, v66
	global_store_dword v64, v0, s[0:1] offset:1024
	global_store_dword v64, v16, s[0:1] offset:1056
	global_store_dword v64, v32, s[0:1] offset:1088
	global_store_dword v64, v48, s[0:1] offset:1120
	s_add_u32 s0, s0, 0x4000
	s_addc_u32 s1, s1, 0
	v_mul_f32_e32 v4, v4, v72
	v_mul_f32_e32 v20, v20, v72
	v_mul_f32_e32 v36, v36, v72
	v_mul_f32_e32 v52, v52, v72
	v_mul_f32_e32 v5, v5, v73
	v_mul_f32_e32 v21, v21, v73
	v_mul_f32_e32 v37, v37, v73
	v_mul_f32_e32 v53, v53, v73
	v_mul_f32_e32 v6, v6, v74
	v_mul_f32_e32 v22, v22, v74
	v_mul_f32_e32 v38, v38, v74
	v_mul_f32_e32 v54, v54, v74
	v_mul_f32_e32 v7, v7, v75
	v_mul_f32_e32 v23, v23, v75
	v_mul_f32_e32 v39, v39, v75
	v_mul_f32_e32 v55, v55, v75
	v_cvt_pk_fp8_f32 v4, v4, v5
	v_cvt_pk_fp8_f32 v20, v20, v21
	v_cvt_pk_fp8_f32 v36, v36, v37
	v_cvt_pk_fp8_f32 v52, v52, v53
	v_cvt_pk_fp8_f32 v4, v6, v7 op_sel:[0,0,1]
	v_cvt_pk_fp8_f32 v20, v22, v23 op_sel:[0,0,1]
	v_cvt_pk_fp8_f32 v36, v38, v39 op_sel:[0,0,1]
	v_cvt_pk_fp8_f32 v52, v54, v55 op_sel:[0,0,1]
	v_mov_b32_dpp v5, v4 quad_perm:[1,0,3,2] row_mask:0xf bank_mask:0xf
	v_mov_b32_dpp v21, v20 quad_perm:[1,0,3,2] row_mask:0xf bank_mask:0xf
	v_mov_b32_dpp v37, v36 quad_perm:[1,0,3,2] row_mask:0xf bank_mask:0xf
; __device__ __forceinline__ bf16_t f2bf(float f) { return (bf16_t)(cvtpk(f, f) & 0xffffu); }
; __device__ __forceinline__ unsigned char f2fp8(float v) { return (unsigned char)(__builtin_amdgcn_cvt_pk_fp8_f32(v, v, (int)__float_as_uint(v), false) & 0xff); }
; __device__ __forceinline__ int crow(int r, int hi) { return (r & 3) + 8 * (r >> 2) + 4 * hi; }
; template <int NKS, bool MACC>
; __device__ __forceinline__ void attn_dense8_dma(int wv, const D8Args a, LAS unsigned char* ldsl) {
;     ...
;     for (int r = 0; r < 16; ++r) { const int orow = da::crow(r, hie);
; #pragma unroll
;         for (int d0 = 0; d0 < 4; ++d0) { if constexpr (F8_OUT) ((unsigned char*)Ow)[(long)orow * a.ldo + d0 * 32 + r32e] = f2fp8(o[d0][r] * rli[r] * O8_SCALE); else Ow[(long)orow * a.ldo + d0 * 32 + r32e] = f2bf(o[d0][r] * rli[r]); } }
; __global__ void __launch_bounds__(NTHR, 2) fwd(Params p) {
;     ...
;                 for (int u = vcu; u < 1024; u += G) {
	v_mov_b32_dpp v53, v52 quad_perm:[1,0,3,2] row_mask:0xf bank_mask:0xf
	v_perm_b32 v6, v5, v4, v65
	v_perm_b32 v22, v21, v20, v65
	v_perm_b32 v38, v37, v36, v65
	v_perm_b32 v54, v53, v52, v65
	v_mov_b32_dpp v7, v6 quad_perm:[2,3,0,1] row_mask:0xf bank_mask:0xf
	v_mov_b32_dpp v23, v22 quad_perm:[2,3,0,1] row_mask:0xf bank_mask:0xf
	v_mov_b32_dpp v39, v38 quad_perm:[2,3,0,1] row_mask:0xf bank_mask:0xf
	v_mov_b32_dpp v55, v54 quad_perm:[2,3,0,1] row_mask:0xf bank_mask:0xf
	v_perm_b32 v4, v7, v6, v66
	v_perm_b32 v20, v23, v22, v66
	v_perm_b32 v36, v39, v38, v66
	v_perm_b32 v52, v55, v54, v66
	global_store_dword v64, v4, s[0:1] offset:1024
	global_store_dword v64, v20, s[0:1] offset:1056
	global_store_dword v64, v36, s[0:1] offset:1088
	global_store_dword v64, v52, s[0:1] offset:1120
	s_add_u32 s0, s0, 0x4000
	s_addc_u32 s1, s1, 0
	v_mul_f32_e32 v8, v8, v76
	v_mul_f32_e32 v24, v24, v76
	v_mul_f32_e32 v40, v40, v76
	v_mul_f32_e32 v56, v56, v76
	v_mul_f32_e32 v9, v9, v77
	v_mul_f32_e32 v25, v25, v77
	v_mul_f32_e32 v41, v41, v77
	v_mul_f32_e32 v57, v57, v77
	v_mul_f32_e32 v10, v10, v78
	v_mul_f32_e32 v26, v26, v78
	v_mul_f32_e32 v42, v42, v78
	v_mul_f32_e32 v58, v58, v78
	v_mul_f32_e32 v11, v11, v79
	v_mul_f32_e32 v27, v27, v79
	v_mul_f32_e32 v43, v43, v79
	v_mul_f32_e32 v59, v59, v79
	v_cvt_pk_fp8_f32 v8, v8, v9
	v_cvt_pk_fp8_f32 v24, v24, v25
	v_cvt_pk_fp8_f32 v40, v40, v41
	v_cvt_pk_fp8_f32 v56, v56, v57
	v_cvt_pk_fp8_f32 v8, v10, v11 op_sel:[0,0,1]
	v_cvt_pk_fp8_f32 v24, v26, v27 op_sel:[0,0,1]
	v_cvt_pk_fp8_f32 v40, v42, v43 op_sel:[0,0,1]
	v_cvt_pk_fp8_f32 v56, v58, v59 op_sel:[0,0,1]
	v_mov_b32_dpp v9, v8 quad_perm:[1,0,3,2] row_mask:0xf bank_mask:0xf
	v_mov_b32_dpp v25, v24 quad_perm:[1,0,3,2] row_mask:0xf bank_mask:0xf
	v_mov_b32_dpp v41, v40 quad_perm:[1,0,3,2] row_mask:0xf bank_mask:0xf
	v_mov_b32_dpp v57, v56 quad_perm:[1,0,3,2] row_mask:0xf bank_mask:0xf
	v_perm_b32 v10, v9, v8, v65
	v_perm_b32 v26, v25, v24, v65
	v_perm_b32 v42, v41, v40, v65
	v_perm_b32 v58, v57, v56, v65
	v_mov_b32_dpp v11, v10 quad_perm:[2,3,0,1] row_mask:0xf bank_mask:0xf
	v_mov_b32_dpp v27, v26 quad_perm:[2,3,0,1] row_mask:0xf bank_mask:0xf
	v_mov_b32_dpp v43, v42 quad_perm:[2,3,0,1] row_mask:0xf bank_mask:0xf
	v_mov_b32_dpp v59, v58 quad_perm:[2,3,0,1] row_mask:0xf bank_mask:0xf
	v_perm_b32 v8, v11, v10, v66
	v_perm_b32 v24, v27, v26, v66
	v_perm_b32 v40, v43, v42, v66
	v_perm_b32 v56, v59, v58, v66
	global_store_dword v64, v8, s[0:1] offset:1024
	global_store_dword v64, v24, s[0:1] offset:1056
	global_store_dword v64, v40, s[0:1] offset:1088
	global_store_dword v64, v56, s[0:1] offset:1120
	s_add_u32 s0, s0, 0x4000
	s_addc_u32 s1, s1, 0
	v_mul_f32_e32 v12, v12, v80
	v_mul_f32_e32 v28, v28, v80
	v_mul_f32_e32 v44, v44, v80
	v_mul_f32_e32 v60, v60, v80
	v_mul_f32_e32 v13, v13, v81
	v_mul_f32_e32 v29, v29, v81
	v_mul_f32_e32 v45, v45, v81
	v_mul_f32_e32 v61, v61, v81
	v_mul_f32_e32 v14, v14, v82
	v_mul_f32_e32 v30, v30, v82
	v_mul_f32_e32 v46, v46, v82
	v_mul_f32_e32 v62, v62, v82
	v_mul_f32_e32 v15, v15, v83
	v_mul_f32_e32 v31, v31, v83
	v_mul_f32_e32 v47, v47, v83
	v_mul_f32_e32 v63, v63, v83
	v_cvt_pk_fp8_f32 v12, v12, v13
	v_cvt_pk_fp8_f32 v28, v28, v29
	v_cvt_pk_fp8_f32 v44, v44, v45
	v_cvt_pk_fp8_f32 v60, v60, v61
	v_cvt_pk_fp8_f32 v12, v14, v15 op_sel:[0,0,1]
	v_cvt_pk_fp8_f32 v28, v30, v31 op_sel:[0,0,1]
	v_cvt_pk_fp8_f32 v44, v46, v47 op_sel:[0,0,1]
	v_cvt_pk_fp8_f32 v60, v62, v63 op_sel:[0,0,1]
	v_mov_b32_dpp v13, v12 quad_perm:[1,0,3,2] row_mask:0xf bank_mask:0xf
	v_mov_b32_dpp v29, v28 quad_perm:[1,0,3,2] row_mask:0xf bank_mask:0xf
	v_mov_b32_dpp v45, v44 quad_perm:[1,0,3,2] row_mask:0xf bank_mask:0xf
	v_mov_b32_dpp v61, v60 quad_perm:[1,0,3,2] row_mask:0xf bank_mask:0xf
	v_perm_b32 v14, v13, v12, v65
	v_perm_b32 v30, v29, v28, v65
	v_perm_b32 v46, v45, v44, v65
	v_perm_b32 v62, v61, v60, v65
	v_mov_b32_dpp v15, v14 quad_perm:[2,3,0,1] row_mask:0xf bank_mask:0xf
	v_mov_b32_dpp v31, v30 quad_perm:[2,3,0,1] row_mask:0xf bank_mask:0xf
	v_mov_b32_dpp v47, v46 quad_perm:[2,3,0,1] row_mask:0xf bank_mask:0xf
	v_mov_b32_dpp v63, v62 quad_perm:[2,3,0,1] row_mask:0xf bank_mask:0xf
	v_perm_b32 v12, v15, v14, v66
	v_perm_b32 v28, v31, v30, v66
	v_perm_b32 v44, v47, v46, v66
	v_perm_b32 v60, v63, v62, v66
	global_store_dword v64, v12, s[0:1] offset:1024
	global_store_dword v64, v28, s[0:1] offset:1056
	global_store_dword v64, v44, s[0:1] offset:1088
	global_store_dword v64, v60, s[0:1] offset:1120
	s_add_i32 s54, s54, s50
	s_cmpk_gt_i32 s54, 0x3ff
	s_cbranch_scc1 .LBB0_483
